# speedup vs baseline: 1.0122x; 1.0122x over previous
.LBB1_21:
	s_or_b64 exec, exec, s[4:5]
	s_lshr_b32 s4, s18, 16
	v_cvt_f32_u32_e32 v3, s4
	v_lshlrev_b64 v[8:9], 11, v[6:7]
	v_lshl_add_u64 v[8:9], s[16:17], 0, v[8:9]
	s_and_b32 s10, s18, 0xffff
	v_lshrrev_b32_e32 v24, 3, v2
	v_lshlrev_b32_e32 v24, 2, v24
	v_add_u32_e32 v25, 32, v24
	ds_bpermute_b32 v32, v24, v16
	ds_bpermute_b32 v33, v25, v16
	v_div_scale_f32 v4, s[4:5], v3, v3, 1.0
	v_rcp_f32_e32 v12, v4
	v_div_scale_f32 v13, vcc, 1.0, v3, 1.0
	v_and_b32_e32 v34, 7, v2
	v_fma_f32 v17, -v4, v12, 1.0
	v_fmac_f32_e32 v12, v17, v12
	v_mul_f32_e32 v17, v13, v12
	v_fma_f32 v18, -v4, v17, v13
	v_fmac_f32_e32 v17, v18, v12
	v_fma_f32 v4, -v4, v17, v13
	v_lshlrev_b32_e32 v34, 2, v34
	v_div_fmas_f32 v4, v4, v12, v17
	v_div_fixup_f32 v4, v4, v3, 1.0
	v_mov_b32_e32 v3, 0
	v_lshl_add_u64 v[8:9], v[2:3], 4, v[8:9]
	s_waitcnt lgkmcnt(0)
	v_lshrrev_b32_e32 v32, v34, v32
	v_lshrrev_b32_e32 v33, v34, v33
	v_bfe_i32 v24, v32, 0, 1
	v_bfe_i32 v25, v32, 1, 1
	v_bfe_i32 v26, v32, 2, 1
	v_bfe_i32 v27, v32, 3, 1
	v_and_b32_e32 v24, v24, v4
	v_and_b32_e32 v25, v25, v4
	v_and_b32_e32 v26, v26, v4
	v_and_b32_e32 v27, v27, v4
	global_store_dwordx4 v[8:9], v[24:27], off
	v_bfe_i32 v28, v33, 0, 1
	v_bfe_i32 v29, v33, 1, 1
	v_bfe_i32 v30, v33, 2, 1
	v_bfe_i32 v31, v33, 3, 1
	v_and_b32_e32 v28, v28, v4
	v_and_b32_e32 v29, v29, v4
	v_and_b32_e32 v30, v30, v4
	v_and_b32_e32 v31, v31, v4
	global_store_dwordx4 v[8:9], v[28:31], off offset:1024
	v_cmp_le_u32_e64 s[4:5], s10, v2
	v_cmp_gt_u32_e32 vcc, 24, v2
	s_and_b64 s[14:15], vcc, s[4:5]
	s_and_saveexec_b64 s[4:5], s[14:15]
	s_cbranch_execz .LBB1_23
	v_mad_u64_u32 v[8:9], s[8:9], v6, 48, s[8:9]
	v_mad_u32_u24 v9, v7, 48, v9
	v_add_u32_e32 v12, -10, v2
	v_cmp_gt_u32_e32 vcc, 4, v12
	s_nop 1
	v_cndmask_b32_e64 v12, 0, 6, vcc
	v_xor_b32_e32 v12, v2, v12
	v_mov_b32_e32 v13, 0
	v_lshl_add_u64 v[8:9], v[12:13], 1, v[8:9]
	v_mov_b32_e32 v3, 0x2000
	global_store_short v[8:9], v3, off
